# hybrid K1 with 12 private chunks per wave (1/3 of the matrix from the queues) + final/agg2 hoists
# baseline (speedup 1.0000x reference)
.Lk1_scan:
	s_load_dwordx2 s[4:5], s[0:1], 0x0
	s_load_dwordx4 s[8:11], s[0:1], 0x20
	s_load_dwordx2 s[12:13], s[0:1], 0x30
	v_and_b32_e32 v6, 63, v0
	v_readfirstlane_b32 s3, v0
	v_lshlrev_b32_e32 v1, 4, v6
	v_lshlrev_b32_e32 v2, 2, v6
	v_or_b32_e32 v3, 1, v2
	v_or_b32_e32 v4, 2, v2
	v_or_b32_e32 v5, 3, v2
	s_lshr_b32 s3, s3, 6
	s_sub_u32 s16, s2, 0x60
	s_lshl_b32 s16, s16, 2
	s_add_u32 s16, s16, s3
	s_mul_i32 s17, s16, 0x48000
	s_lshr_b32 s18, s17, 2
	s_lshl_b32 s24, s3, 13
	s_mov_b32 s25, s24
	s_mov_b32 s28, s24
	s_mov_b32 s36, 0
	v_mov_b32_e32 v21, 1
	s_mov_b32 s27, 0
	s_mov_b32 s29, 0x55555556
	s_mov_b32 s31, 0xc0000
	s_waitcnt lgkmcnt(0)
	s_and_b32 s50, s16, 15
	s_mul_i32 s52, s50, 768
	s_add_u32 s52, s52, 24576
	s_lshl_b32 s53, s50, 6
	s_add_u32 s53, s53, 0xe000
	s_add_u32 s54, s10, s53
	s_addc_u32 s55, s11, 0
	s_mul_i32 s59, s16, 12
	s_mul_i32 s57, s59, 0x4000
	s_lshr_b32 s18, s57, 2
	s_add_u32 s6, s4, s57
	s_addc_u32 s7, s5, 0
	v_mov_b32_e32 v27, 0
	global_load_dwordx4 v[28:31], v1, s[6:7] nt
	s_add_u32 s6, s6, 0x400
	s_addc_u32 s7, s7, 0
	global_load_dwordx4 v[32:35], v1, s[6:7] nt
	s_add_u32 s6, s6, 0x400
	s_addc_u32 s7, s7, 0
	global_load_dwordx4 v[36:39], v1, s[6:7] nt
	s_add_u32 s6, s6, 0x400
	s_addc_u32 s7, s7, 0
	global_load_dwordx4 v[40:43], v1, s[6:7] nt
	s_add_u32 s6, s6, 0x400
	s_addc_u32 s7, s7, 0
	global_load_dwordx4 v[44:47], v1, s[6:7] nt
	s_add_u32 s6, s6, 0x400
	s_addc_u32 s7, s7, 0
	global_load_dwordx4 v[48:51], v1, s[6:7] nt
	s_add_u32 s6, s6, 0x400
	s_addc_u32 s7, s7, 0
	global_load_dwordx4 v[52:55], v1, s[6:7] nt
	s_add_u32 s6, s6, 0x400
	s_addc_u32 s7, s7, 0
	global_load_dwordx4 v[56:59], v1, s[6:7] nt
	s_add_u32 s6, s6, 0x400
	s_addc_u32 s7, s7, 0
	global_load_dwordx4 v[60:63], v1, s[6:7] nt
	s_add_u32 s6, s6, 0x400
	s_addc_u32 s7, s7, 0
	global_load_dwordx4 v[64:67], v1, s[6:7] nt
	s_add_u32 s6, s6, 0x400
	s_addc_u32 s7, s7, 0
	global_load_dwordx4 v[68:71], v1, s[6:7] nt
	s_add_u32 s6, s6, 0x400
	s_addc_u32 s7, s7, 0
	global_load_dwordx4 v[72:75], v1, s[6:7] nt
	s_add_u32 s6, s6, 0x400
	s_addc_u32 s7, s7, 0
	global_load_dwordx4 v[76:79], v1, s[6:7] nt
	s_add_u32 s6, s6, 0x400
	s_addc_u32 s7, s7, 0
	global_load_dwordx4 v[80:83], v1, s[6:7] nt
	s_add_u32 s6, s6, 0x400
	s_addc_u32 s7, s7, 0
	global_load_dwordx4 v[84:87], v1, s[6:7] nt
	s_add_u32 s6, s6, 0x400
	s_addc_u32 s7, s7, 0
	global_load_dwordx4 v[88:91], v1, s[6:7] nt
	s_add_u32 s6, s6, 0x400
	s_addc_u32 s7, s7, 0
	s_mov_b32 s26, 18
	s_add_u32 s57, s59, 1
	s_mul_i32 s57, s57, 0x4000
	s_lshr_b32 s58, s57, 2
	s_add_u32 s6, s4, s57
	s_addc_u32 s7, s5, 0
	s_mov_b32 s26, 0

.Lk1_contm_15:
	global_load_dwordx4 v[60:63], v1, s[6:7] nt
	s_add_u32 s6, s6, 0x400
	s_addc_u32 s7, s7, 0
	global_load_dwordx4 v[64:67], v1, s[6:7] nt
	s_add_u32 s6, s6, 0x400
	s_addc_u32 s7, s7, 0
	global_load_dwordx4 v[68:71], v1, s[6:7] nt
	s_add_u32 s6, s6, 0x400
	s_addc_u32 s7, s7, 0
	global_load_dwordx4 v[72:75], v1, s[6:7] nt
	s_add_u32 s6, s6, 0x400
	s_addc_u32 s7, s7, 0
	global_load_dwordx4 v[76:79], v1, s[6:7] nt
	s_add_u32 s6, s6, 0x400
	s_addc_u32 s7, s7, 0
	global_load_dwordx4 v[80:83], v1, s[6:7] nt
	s_add_u32 s6, s6, 0x400
	s_addc_u32 s7, s7, 0
	global_load_dwordx4 v[84:87], v1, s[6:7] nt
	s_add_u32 s6, s6, 0x400
	s_addc_u32 s7, s7, 0
	global_load_dwordx4 v[88:91], v1, s[6:7] nt
	s_add_u32 s6, s6, 0x400
	s_addc_u32 s7, s7, 0
	s_mov_b32 s18, s58
	s_add_u32 s60, s26, 2
	s_cmp_lt_u32 s60, 12
	s_cbranch_scc0 .Lk1_dynid
	s_add_u32 s57, s59, s60
	s_branch .Lk1_haveid
.Lk1_dynid:
	v_readfirstlane_b32 s56, v26
	s_nop 0
	s_cmp_lt_u32 s56, 768
	s_cbranch_scc0 .Lk1_lastchunk
	s_add_u32 s57, s52, s56
.Lk1_haveid:
	s_mul_i32 s57, s57, 0x4000
	s_lshr_b32 s58, s57, 2
	s_add_u32 s6, s4, s57
	s_addc_u32 s7, s5, 0
	s_add_u32 s60, s26, 3
	s_cmp_lt_u32 s60, 12
	s_cbranch_scc1 .Lk1_noreq
	s_mov_b64 exec, 1
	global_atomic_add v26, v27, v21, s[54:55] sc0
	s_mov_b64 exec, -1
